# conversion-first loop: queue atomic issued without waiting, its result consumed before the transpose barrier; slab loads back at the loop top
# speedup vs baseline: 1.0259x; 1.0014x over previous
; #define CQ_LOAD(buf, slab, src, ldw) do { _Pragma("unroll") for (int r_ = 0; r_ < 4; ++r_) a[buf][r_] = __builtin_nontemporal_load((const f32x4*)(src + (size_t)((slab) * 32 + r_) * ldw)); } while (0)
; __device__ __forceinline__ void conv_queue(const P& p, LAS unsigned char* lds, int* ctr, int max_tiles) {
;     ...
;     for (int it = 0;; ++it) {
;         const bool more = t_nxt < NMT, cur_w1 = t_cur < NM1;
;         if (tid == 0) qs[1 + (it & 1)] = (more && CQ_CAN) ? atomicAdd(ctr, 1) : NMT;
;     ...
;         CQ_LOAD(2, 2, s1, l1); CQ_LOAD(3, 3, s1, l1);
.LBB0_818:
	s_mov_b32 s98, 0
	s_mov_b32 s99, 0
	global_load_dwordx4 v[52:55], v[2:3], off nt
	global_load_dwordx4 v[56:59], v[4:5], off nt
	global_load_dwordx4 v[60:63], v[6:7], off nt
	global_load_dwordx4 v[64:67], v[8:9], off nt
	global_load_dwordx4 v[2:5], v[10:11], off nt
	global_load_dwordx4 v[6:9], v[12:13], off nt
	global_load_dwordx4 v[10:13], v[14:15], off nt
	s_nop 0
	global_load_dwordx4 v[14:17], v[16:17], off nt
	v_mov_b32_e32 v18, s11
	ds_read_b32 v18, v18
	s_waitcnt lgkmcnt(0)
	v_readfirstlane_b32 s25, v18
	s_cmpk_lt_i32 s25, 0x3000
	s_cselect_b64 s[10:11], -1, 0
	v_cndmask_b32_e64 v18, 0, 1, s[10:11]
	v_cmp_ne_u32_e64 s[4:5], 1, v18
	s_mov_b64 s[6:7], exec
	v_readlane_b32 s12, v242, 31
	v_readlane_b32 s13, v242, 32
	s_and_b64 s[12:13], s[6:7], s[12:13]
	s_mov_b64 exec, s[12:13]
	s_cbranch_execz .LBB0_824
	s_and_b64 vcc, exec, s[4:5]
	v_mov_b32_e32 v18, 0x3000
	s_cbranch_vccnz .LBB0_823
	s_mov_b64 s[14:15], exec
	v_mbcnt_lo_u32_b32 v18, s14, 0
	v_mbcnt_hi_u32_b32 v18, s15, v18
	v_cmp_eq_u32_e32 vcc, 0, v18
	s_and_saveexec_b64 s[12:13], vcc
	s_cbranch_execz .LBB0_822
	s_bcnt1_i32_b64 s8, s[14:15]
	v_mov_b32_e32 v243, s8
	global_atomic_add v243, v19, v243, s[0:1] sc0
	s_mov_b32 s99, 1

; #define CQ_LOAD(buf, slab, src, ldw) do { _Pragma("unroll") for (int r_ = 0; r_ < 4; ++r_) a[buf][r_] = __builtin_nontemporal_load((const f32x4*)(src + (size_t)((slab) * 32 + r_) * ldw)); } while (0)
; __device__ __forceinline__ void conv_queue(const P& p, LAS unsigned char* lds, int* ctr, int max_tiles) {
;     ...
;     { CQ_SRC(t_cur, s0, l0); CQ_LOAD(0, 0, s0, l0); CQ_LOAD(1, 1, s0, l0); CQ_LOAD(2, 2, s0, l0); CQ_LOAD(3, 3, s0, l0); }
;     for (int it = 0;; ++it) {
;         const bool more = t_nxt < NMT, cur_w1 = t_cur < NM1;
;         if (tid == 0) qs[1 + (it & 1)] = (more && CQ_CAN) ? atomicAdd(ctr, 1) : NMT;
;         ++pulled;
;         CQ_PUT(0, 0); CQ_PUT(1, 1);
.LBB0_823:
.LBB0_824:
	s_or_b64 exec, exec, s[6:7]
	s_cmpk_lt_i32 s26, 0x2000
	s_cselect_b64 s[16:17], -1, 0
	s_cmpk_gt_i32 s26, 0x1fff
	s_cselect_b64 s[14:15], -1, 0
	s_mov_b64 s[6:7], -1
	s_and_b64 vcc, exec, s[16:17]
	v_add_u32_e32 v18, 0x4000, v82
	s_cbranch_vccnz .LBB0_826
	v_mov_b32_e32 v73, v19
	v_mov_b32_e32 v74, v19
	s_waitcnt vmcnt(14)
	v_cvt_scalef32_pk_fp8_f32 v73, v20, v24, s23
	v_cvt_scalef32_pk_fp8_f32 v74, v21, v25, s23
	s_waitcnt vmcnt(12)
	v_cvt_scalef32_pk_fp8_f32 v73, v28, v32, s23 op_sel:[0,0,0,1]
	v_cvt_scalef32_pk_fp8_f32 v74, v29, v33, s23 op_sel:[0,0,0,1]
	ds_write2_b32 v18, v73, v74 offset1:33
	v_mov_b32_e32 v73, v19
	v_mov_b32_e32 v74, v19
	v_cvt_scalef32_pk_fp8_f32 v73, v22, v26, s23
	v_cvt_scalef32_pk_fp8_f32 v74, v23, v27, s23
	v_cvt_scalef32_pk_fp8_f32 v73, v30, v34, s23 op_sel:[0,0,0,1]
	v_cvt_scalef32_pk_fp8_f32 v74, v31, v35, s23 op_sel:[0,0,0,1]
	s_mov_b64 s[6:7], 0
	ds_write2_b32 v18, v73, v74 offset0:66 offset1:99

; #define LAS __attribute__((address_space(3)))
; __device__ __forceinline__ void conv_queue(const P& p, LAS unsigned char* lds, int* ctr, int max_tiles) {
;     ...
;         if (tid == 0) qs[1 + (it & 1)] = (more && CQ_CAN) ? atomicAdd(ctr, 1) : NMT;
;     ...
;         __syncthreads();
;         { const int t2_ = cur_w1 ? t_cur : t_cur - NM1, e_ = cur_w1 ? t2_ >> 8 : t2_ >> 7, r_ = cur_w1 ? t2_ & 255 : t2_ & 127;
;           const int k0 = (cur_w1 ? r_ >> 4 : r_ >> 3) * 128, n0 = (cur_w1 ? r_ & 15 : r_ & 7) * 256;
;           if (cur_w1) {
;               unsigned char* Bt = p.ws + WS_W1_T + (size_t)e_ * 4096 * 2048;
; #pragma unroll 1
;               for (int ps = 0; ps < 2; ++ps) { const int id = tid + 512 * ps, n = id >> 2, q = id & 3; const LAS u32x2* tp_ = (const LAS u32x2*)(Tb + n * 264 + q * 64);
;                   u32x16 wv;
; #pragma unroll
;                   for (int i = 0; i < 8; ++i) { const u32x2 w = tp_[i]; wv[2 * i] = w.x; wv[2 * i + 1] = w.y; }
;                   u32x4 lo, hi; fp6_block_bf16(wv, lo, hi);
;                   unsigned char* dst = Bt + (size_t)DmW1{}(n0 + n) * 2048 + k0 + 16 * q;
;                   __builtin_nontemporal_store(lo, (u32x4*)dst); __builtin_nontemporal_store(hi, (u32x4*)(dst + 64)); }
;           } else {
;               unsigned char* Bt = p.ws + WS_W2_T + (size_t)e_ * 2048 * 2048;
; #pragma unroll
;               for (int ps = 0; ps < 4; ++ps) { const int n = ps * 64 + (tid >> 3), c = tid & 7; const LAS unsigned* tp_ = (const LAS unsigned*)(Tb + n * 132 + 16 * c);
;                   u32x4 w; w.x = tp_[0]; w.y = tp_[1]; w.z = tp_[2]; w.w = tp_[3];
;                   __builtin_nontemporal_store(w, (u32x4*)(Bt + (size_t)(n0 + n) * 2048 + k0 + 16 * c)); }
.LBB0_846:
	s_mov_b64 s[100:101], exec
	v_readlane_b32 vcc_lo, v242, 31
	v_readlane_b32 vcc_hi, v242, 32
	s_and_b64 exec, exec, vcc
	s_cbranch_execz .Lcq_dskip
	v_mov_b32_e32 v244, 0x3000
	s_cmp_eq_u32 s99, 0
	s_cbranch_scc1 .Lcq_dnoat
	v_readfirstlane_b32 s99, v243
	s_nop 1
	v_mov_b32_e32 v244, s99
.Lcq_dnoat:
	s_and_b32 s99, s24, 1
	s_lshl_b32 s99, s99, 2
	s_add_i32 s99, s99, 0x16464
	v_mov_b32_e32 v243, s99
	ds_write_b32 v243, v244
.Lcq_dskip:
	s_mov_b64 exec, s[100:101]
	s_add_i32 s13, s26, 0xffffe000
	s_and_b64 s[16:17], exec, s[16:17]
	s_cselect_b32 s13, s26, s13
	s_and_b32 s7, s7, s13
	s_lshr_b32 s7, s7, s11
	s_ashr_i32 s6, s13, s6
	s_lshl_b32 s11, s7, 7
	s_and_b32 s7, s8, s13
	s_lshl_b32 s8, s7, 8
	s_ashr_i32 s7, s6, 31
	s_mov_b64 s[16:17], -1
	s_and_b64 vcc, exec, s[14:15]
	s_waitcnt lgkmcnt(0)
	s_barrier
	s_cbranch_vccz .LBB0_848
	s_lshl_b64 s[14:15], s[6:7], 22
	s_add_u32 s13, s3, s14
	v_add_u32_e32 v2, 0x4000, v81
	v_add_u32_e32 v4, 0x4008, v81
	s_addc_u32 s15, s20, s15
	ds_read2_b32 v[2:3], v2 offset1:1
	ds_read2_b32 v[4:5], v4 offset1:1
	s_add_u32 s14, s13, s11
	v_or_b32_e32 v6, s8, v76
	s_addc_u32 s15, s15, 0
	v_lshlrev_b32_e32 v18, 11, v6
	v_add_u32_e32 v6, 0x6100, v81
	v_add_u32_e32 v8, 0x6108, v81
	v_lshl_add_u64 v[10:11], s[14:15], 0, v[68:69]
	ds_read2_b32 v[6:7], v6 offset1:1
	ds_read2_b32 v[8:9], v8 offset1:1
	v_lshl_add_u64 v[12:13], v[10:11], 0, v[18:19]
	s_waitcnt lgkmcnt(2)
	global_store_dwordx4 v[12:13], v[2:5], off nt
	s_mov_b64 s[16:17], 0
	s_nop 0
	v_or_b32_e32 v2, s8, v78
	v_lshlrev_b32_e32 v18, 11, v2
	v_lshl_add_u64 v[2:3], v[10:11], 0, v[18:19]
	s_waitcnt lgkmcnt(0)
	global_store_dwordx4 v[2:3], v[6:9], off nt
	v_add_u32_e32 v2, 0x8200, v81
	v_add_u32_e32 v4, 0x8208, v81
	v_or_b32_e32 v6, s8, v79
	ds_read2_b32 v[2:3], v2 offset1:1
	ds_read2_b32 v[4:5], v4 offset1:1
	v_lshlrev_b32_e32 v18, 11, v6
	v_add_u32_e32 v6, 0xa300, v81
	v_add_u32_e32 v8, 0xa308, v81
	ds_read2_b32 v[6:7], v6 offset1:1
	ds_read2_b32 v[8:9], v8 offset1:1
	v_lshl_add_u64 v[12:13], v[10:11], 0, v[18:19]
	v_add_lshl_u32 v18, s8, v80, 11
	s_waitcnt lgkmcnt(2)
	global_store_dwordx4 v[12:13], v[2:5], off nt
	s_nop 1
	v_lshl_add_u64 v[2:3], v[10:11], 0, v[18:19]
	s_waitcnt lgkmcnt(0)
	global_store_dwordx4 v[2:3], v[6:9], off nt
